# CSR sort uses finer column windows: window = (col*223)>>20 (32 windows of ~4700 rows over all nodes) instead of col>>13
# speedup vs baseline: 1.0847x; 1.0021x over previous
.LBB3_46:
	s_and_b64 vcc, exec, s[0:1]
	s_cbranch_vccz .LBB3_141
	s_ashr_i32 s37, s36, 31
	s_lshl_b64 s[0:1], s[36:37], 3
	s_add_u32 s0, s2, s0
	s_addc_u32 s1, s3, s1
	s_add_i32 s8, s44, 31
	s_lshr_b32 s8, s8, 5
	s_add_i32 s8, s8, -1
	s_lshl_b32 s9, s42, 2
	s_sub_i32 s8, s8, s9
	s_bfe_u32 s8, s8, 0x1000a
	s_mul_i32 s8, s8, 31
	v_mov_b32_e32 v50, 0
	v_mov_b32_e32 v51, 0
	v_mov_b32_e32 v52, 0
	v_mov_b32_e32 v53, 0
	v_lshlrev_b32_e32 v1, 4, v0
	ds_write_b128 v1, v[50:53]
	v_mov_b32_e32 v63, 1
	v_add_u32_e32 v54, 0, v0
	v_lshl_add_u32 v54, v54, 1, 0
	v_cmp_gt_i32_e32 vcc, s33, v54
	v_lshlrev_b32_e32 v54, 3, v54
	s_and_saveexec_b64 s[4:5], vcc
	global_load_dwordx4 v[2:5], v54, s[0:1]
	s_or_b64 exec, exec, s[4:5]
	v_add_u32_e32 v54, 1024, v0
	v_lshl_add_u32 v54, v54, 1, 0
	v_cmp_gt_i32_e32 vcc, s33, v54
	v_lshlrev_b32_e32 v54, 3, v54
	s_and_saveexec_b64 s[4:5], vcc
	global_load_dwordx4 v[6:9], v54, s[0:1]
	s_or_b64 exec, exec, s[4:5]
	v_add_u32_e32 v54, 2048, v0
	v_lshl_add_u32 v54, v54, 1, 0
	v_cmp_gt_i32_e32 vcc, s33, v54
	v_lshlrev_b32_e32 v54, 3, v54
	s_and_saveexec_b64 s[4:5], vcc
	global_load_dwordx4 v[10:13], v54, s[0:1]
	s_or_b64 exec, exec, s[4:5]
	v_add_u32_e32 v54, 3072, v0
	v_lshl_add_u32 v54, v54, 1, 0
	v_cmp_gt_i32_e32 vcc, s33, v54
	v_lshlrev_b32_e32 v54, 3, v54
	s_and_saveexec_b64 s[4:5], vcc
	global_load_dwordx4 v[14:17], v54, s[0:1]
	s_or_b64 exec, exec, s[4:5]
	v_add_u32_e32 v54, 4096, v0
	v_lshl_add_u32 v54, v54, 1, 0
	v_cmp_gt_i32_e32 vcc, s33, v54
	v_lshlrev_b32_e32 v54, 3, v54
	s_and_saveexec_b64 s[4:5], vcc
	global_load_dwordx4 v[18:21], v54, s[0:1]
	s_or_b64 exec, exec, s[4:5]
	v_add_u32_e32 v54, 5120, v0
	v_lshl_add_u32 v54, v54, 1, 0
	v_cmp_gt_i32_e32 vcc, s33, v54
	v_lshlrev_b32_e32 v54, 3, v54
	s_and_saveexec_b64 s[4:5], vcc
	global_load_dwordx4 v[22:25], v54, s[0:1]
	s_or_b64 exec, exec, s[4:5]
	v_add_u32_e32 v54, 6144, v0
	v_lshl_add_u32 v54, v54, 1, 0
	v_cmp_gt_i32_e32 vcc, s33, v54
	v_lshlrev_b32_e32 v54, 3, v54
	s_and_saveexec_b64 s[4:5], vcc
	global_load_dwordx4 v[26:29], v54, s[0:1]
	s_or_b64 exec, exec, s[4:5]
	v_add_u32_e32 v54, 7168, v0
	v_lshl_add_u32 v54, v54, 1, 0
	v_cmp_gt_i32_e32 vcc, s33, v54
	v_lshlrev_b32_e32 v54, 3, v54
	s_and_saveexec_b64 s[4:5], vcc
	global_load_dwordx4 v[30:33], v54, s[0:1]
	s_or_b64 exec, exec, s[4:5]
	s_waitcnt lgkmcnt(0)
	s_barrier
	s_waitcnt vmcnt(7)
	v_lshrrev_b32_e32 v54, 25, v2
	v_mul_u32_u24_e32 v55, 0xdf, v2
	v_lshrrev_b32_e32 v55, 20, v55
	v_min_u32_e32 v55, 31, v55
	v_xor_b32_e32 v55, s8, v55
	v_lshl_or_b32 v54, v54, 5, v55
	v_lshlrev_b32_e32 v56, 2, v54
	v_add_u32_e32 v54, 0, v0
	v_lshl_add_u32 v54, v54, 1, 0
	v_cmp_gt_i32_e32 vcc, s33, v54
	s_and_saveexec_b64 s[4:5], vcc
	ds_add_rtn_u32 v34, v56, v63
	s_or_b64 exec, exec, s[4:5]
	s_waitcnt vmcnt(7)
	v_lshrrev_b32_e32 v54, 25, v4
	v_mul_u32_u24_e32 v55, 0xdf, v4
	v_lshrrev_b32_e32 v55, 20, v55
	v_min_u32_e32 v55, 31, v55
	v_xor_b32_e32 v55, s8, v55
	v_lshl_or_b32 v54, v54, 5, v55
	v_lshlrev_b32_e32 v56, 2, v54
	v_add_u32_e32 v54, 0, v0
	v_lshl_add_u32 v54, v54, 1, 1
	v_cmp_gt_i32_e32 vcc, s33, v54
	s_and_saveexec_b64 s[4:5], vcc
	ds_add_rtn_u32 v35, v56, v63
	s_or_b64 exec, exec, s[4:5]
	s_waitcnt vmcnt(6)
	v_lshrrev_b32_e32 v54, 25, v6
	v_mul_u32_u24_e32 v55, 0xdf, v6
	v_lshrrev_b32_e32 v55, 20, v55
	v_min_u32_e32 v55, 31, v55
	v_xor_b32_e32 v55, s8, v55
	v_lshl_or_b32 v54, v54, 5, v55
	v_lshlrev_b32_e32 v56, 2, v54
	v_add_u32_e32 v54, 1024, v0
	v_lshl_add_u32 v54, v54, 1, 0
	v_cmp_gt_i32_e32 vcc, s33, v54
	s_and_saveexec_b64 s[4:5], vcc
	ds_add_rtn_u32 v36, v56, v63
	s_or_b64 exec, exec, s[4:5]
	s_waitcnt vmcnt(6)
	v_lshrrev_b32_e32 v54, 25, v8
	v_mul_u32_u24_e32 v55, 0xdf, v8
	v_lshrrev_b32_e32 v55, 20, v55
	v_min_u32_e32 v55, 31, v55
	v_xor_b32_e32 v55, s8, v55
	v_lshl_or_b32 v54, v54, 5, v55
	v_lshlrev_b32_e32 v56, 2, v54
	v_add_u32_e32 v54, 1024, v0
	v_lshl_add_u32 v54, v54, 1, 1
	v_cmp_gt_i32_e32 vcc, s33, v54
	s_and_saveexec_b64 s[4:5], vcc
	ds_add_rtn_u32 v37, v56, v63
	s_or_b64 exec, exec, s[4:5]
	s_waitcnt vmcnt(5)
	v_lshrrev_b32_e32 v54, 25, v10
	v_mul_u32_u24_e32 v55, 0xdf, v10
	v_lshrrev_b32_e32 v55, 20, v55
	v_min_u32_e32 v55, 31, v55
	v_xor_b32_e32 v55, s8, v55
	v_lshl_or_b32 v54, v54, 5, v55
	v_lshlrev_b32_e32 v56, 2, v54
	v_add_u32_e32 v54, 2048, v0
	v_lshl_add_u32 v54, v54, 1, 0
	v_cmp_gt_i32_e32 vcc, s33, v54
	s_and_saveexec_b64 s[4:5], vcc
	ds_add_rtn_u32 v38, v56, v63
	s_or_b64 exec, exec, s[4:5]
	s_waitcnt vmcnt(5)
	v_lshrrev_b32_e32 v54, 25, v12
	v_mul_u32_u24_e32 v55, 0xdf, v12
	v_lshrrev_b32_e32 v55, 20, v55
	v_min_u32_e32 v55, 31, v55
	v_xor_b32_e32 v55, s8, v55
	v_lshl_or_b32 v54, v54, 5, v55
	v_lshlrev_b32_e32 v56, 2, v54
	v_add_u32_e32 v54, 2048, v0
	v_lshl_add_u32 v54, v54, 1, 1
	v_cmp_gt_i32_e32 vcc, s33, v54
	s_and_saveexec_b64 s[4:5], vcc
	ds_add_rtn_u32 v39, v56, v63
	s_or_b64 exec, exec, s[4:5]
	s_waitcnt vmcnt(4)
	v_lshrrev_b32_e32 v54, 25, v14
	v_mul_u32_u24_e32 v55, 0xdf, v14
	v_lshrrev_b32_e32 v55, 20, v55
	v_min_u32_e32 v55, 31, v55
	v_xor_b32_e32 v55, s8, v55
	v_lshl_or_b32 v54, v54, 5, v55
	v_lshlrev_b32_e32 v56, 2, v54
	v_add_u32_e32 v54, 3072, v0
	v_lshl_add_u32 v54, v54, 1, 0
	v_cmp_gt_i32_e32 vcc, s33, v54
	s_and_saveexec_b64 s[4:5], vcc
	ds_add_rtn_u32 v40, v56, v63
	s_or_b64 exec, exec, s[4:5]
	s_waitcnt vmcnt(4)
	v_lshrrev_b32_e32 v54, 25, v16
	v_mul_u32_u24_e32 v55, 0xdf, v16
	v_lshrrev_b32_e32 v55, 20, v55
	v_min_u32_e32 v55, 31, v55
	v_xor_b32_e32 v55, s8, v55
	v_lshl_or_b32 v54, v54, 5, v55
	v_lshlrev_b32_e32 v56, 2, v54
	v_add_u32_e32 v54, 3072, v0
	v_lshl_add_u32 v54, v54, 1, 1
	v_cmp_gt_i32_e32 vcc, s33, v54
	s_and_saveexec_b64 s[4:5], vcc
	ds_add_rtn_u32 v41, v56, v63
	s_or_b64 exec, exec, s[4:5]
	s_waitcnt vmcnt(3)
	v_lshrrev_b32_e32 v54, 25, v18
	v_mul_u32_u24_e32 v55, 0xdf, v18
	v_lshrrev_b32_e32 v55, 20, v55
	v_min_u32_e32 v55, 31, v55
	v_xor_b32_e32 v55, s8, v55
	v_lshl_or_b32 v54, v54, 5, v55
	v_lshlrev_b32_e32 v56, 2, v54
	v_add_u32_e32 v54, 4096, v0
	v_lshl_add_u32 v54, v54, 1, 0
	v_cmp_gt_i32_e32 vcc, s33, v54
	s_and_saveexec_b64 s[4:5], vcc
	ds_add_rtn_u32 v42, v56, v63
	s_or_b64 exec, exec, s[4:5]
	s_waitcnt vmcnt(3)
	v_lshrrev_b32_e32 v54, 25, v20
	v_mul_u32_u24_e32 v55, 0xdf, v20
	v_lshrrev_b32_e32 v55, 20, v55
	v_min_u32_e32 v55, 31, v55
	v_xor_b32_e32 v55, s8, v55
	v_lshl_or_b32 v54, v54, 5, v55
	v_lshlrev_b32_e32 v56, 2, v54
	v_add_u32_e32 v54, 4096, v0
	v_lshl_add_u32 v54, v54, 1, 1
	v_cmp_gt_i32_e32 vcc, s33, v54
	s_and_saveexec_b64 s[4:5], vcc
	ds_add_rtn_u32 v43, v56, v63
	s_or_b64 exec, exec, s[4:5]
	s_waitcnt vmcnt(2)
	v_lshrrev_b32_e32 v54, 25, v22
	v_mul_u32_u24_e32 v55, 0xdf, v22
	v_lshrrev_b32_e32 v55, 20, v55
	v_min_u32_e32 v55, 31, v55
	v_xor_b32_e32 v55, s8, v55
	v_lshl_or_b32 v54, v54, 5, v55
	v_lshlrev_b32_e32 v56, 2, v54
	v_add_u32_e32 v54, 5120, v0
	v_lshl_add_u32 v54, v54, 1, 0
	v_cmp_gt_i32_e32 vcc, s33, v54
	s_and_saveexec_b64 s[4:5], vcc
	ds_add_rtn_u32 v44, v56, v63
	s_or_b64 exec, exec, s[4:5]
	s_waitcnt vmcnt(2)
	v_lshrrev_b32_e32 v54, 25, v24
	v_mul_u32_u24_e32 v55, 0xdf, v24
	v_lshrrev_b32_e32 v55, 20, v55
	v_min_u32_e32 v55, 31, v55
	v_xor_b32_e32 v55, s8, v55
	v_lshl_or_b32 v54, v54, 5, v55
	v_lshlrev_b32_e32 v56, 2, v54
	v_add_u32_e32 v54, 5120, v0
	v_lshl_add_u32 v54, v54, 1, 1
	v_cmp_gt_i32_e32 vcc, s33, v54
	s_and_saveexec_b64 s[4:5], vcc
	ds_add_rtn_u32 v45, v56, v63
	s_or_b64 exec, exec, s[4:5]
	s_waitcnt vmcnt(1)
	v_lshrrev_b32_e32 v54, 25, v26
	v_mul_u32_u24_e32 v55, 0xdf, v26
	v_lshrrev_b32_e32 v55, 20, v55
	v_min_u32_e32 v55, 31, v55
	v_xor_b32_e32 v55, s8, v55
	v_lshl_or_b32 v54, v54, 5, v55
	v_lshlrev_b32_e32 v56, 2, v54
	v_add_u32_e32 v54, 6144, v0
	v_lshl_add_u32 v54, v54, 1, 0
	v_cmp_gt_i32_e32 vcc, s33, v54
	s_and_saveexec_b64 s[4:5], vcc
	ds_add_rtn_u32 v46, v56, v63
	s_or_b64 exec, exec, s[4:5]
	s_waitcnt vmcnt(1)
	v_lshrrev_b32_e32 v54, 25, v28
	v_mul_u32_u24_e32 v55, 0xdf, v28
	v_lshrrev_b32_e32 v55, 20, v55
	v_min_u32_e32 v55, 31, v55
	v_xor_b32_e32 v55, s8, v55
	v_lshl_or_b32 v54, v54, 5, v55
	v_lshlrev_b32_e32 v56, 2, v54
	v_add_u32_e32 v54, 6144, v0
	v_lshl_add_u32 v54, v54, 1, 1
	v_cmp_gt_i32_e32 vcc, s33, v54
	s_and_saveexec_b64 s[4:5], vcc
	ds_add_rtn_u32 v47, v56, v63
	s_or_b64 exec, exec, s[4:5]
	s_waitcnt vmcnt(0)
	v_lshrrev_b32_e32 v54, 25, v30
	v_mul_u32_u24_e32 v55, 0xdf, v30
	v_lshrrev_b32_e32 v55, 20, v55
	v_min_u32_e32 v55, 31, v55
	v_xor_b32_e32 v55, s8, v55
	v_lshl_or_b32 v54, v54, 5, v55
	v_lshlrev_b32_e32 v56, 2, v54
	v_add_u32_e32 v54, 7168, v0
	v_lshl_add_u32 v54, v54, 1, 0
	v_cmp_gt_i32_e32 vcc, s33, v54
	s_and_saveexec_b64 s[4:5], vcc
	ds_add_rtn_u32 v48, v56, v63
	s_or_b64 exec, exec, s[4:5]
	s_waitcnt vmcnt(0)
	v_lshrrev_b32_e32 v54, 25, v32
	v_mul_u32_u24_e32 v55, 0xdf, v32
	v_lshrrev_b32_e32 v55, 20, v55
	v_min_u32_e32 v55, 31, v55
	v_xor_b32_e32 v55, s8, v55
	v_lshl_or_b32 v54, v54, 5, v55
	v_lshlrev_b32_e32 v56, 2, v54
	v_add_u32_e32 v54, 7168, v0
	v_lshl_add_u32 v54, v54, 1, 1
	v_cmp_gt_i32_e32 vcc, s33, v54
	s_and_saveexec_b64 s[4:5], vcc
	ds_add_rtn_u32 v49, v56, v63
	s_or_b64 exec, exec, s[4:5]
	s_waitcnt lgkmcnt(0)
	s_barrier
	ds_read_b128 v[50:53], v1
	v_mbcnt_lo_u32_b32 v54, -1, 0
	v_mbcnt_hi_u32_b32 v54, -1, v54
	v_lshrrev_b32_e32 v55, 6, v0
	s_waitcnt lgkmcnt(0)
	v_add_u32_e32 v56, v50, v51
	v_add_u32_e32 v57, v56, v52
	v_add_u32_e32 v58, v57, v53
	v_mov_b32_e32 v59, v58
	v_subrev_u32_e32 v61, 1, v54
	v_lshlrev_b32_e32 v61, 2, v61
	ds_bpermute_b32 v60, v61, v59
	v_cmp_le_u32_e32 vcc, 1, v54
	s_waitcnt lgkmcnt(0)
	v_cndmask_b32_e32 v60, 0, v60, vcc
	v_add_u32_e32 v59, v59, v60
	v_subrev_u32_e32 v61, 2, v54
	v_lshlrev_b32_e32 v61, 2, v61
	ds_bpermute_b32 v60, v61, v59
	v_cmp_le_u32_e32 vcc, 2, v54
	s_waitcnt lgkmcnt(0)
	v_cndmask_b32_e32 v60, 0, v60, vcc
	v_add_u32_e32 v59, v59, v60
	v_subrev_u32_e32 v61, 4, v54
	v_lshlrev_b32_e32 v61, 2, v61
	ds_bpermute_b32 v60, v61, v59
	v_cmp_le_u32_e32 vcc, 4, v54
	s_waitcnt lgkmcnt(0)
	v_cndmask_b32_e32 v60, 0, v60, vcc
	v_add_u32_e32 v59, v59, v60
	v_subrev_u32_e32 v61, 8, v54
	v_lshlrev_b32_e32 v61, 2, v61
	ds_bpermute_b32 v60, v61, v59
	v_cmp_le_u32_e32 vcc, 8, v54
	s_waitcnt lgkmcnt(0)
	v_cndmask_b32_e32 v60, 0, v60, vcc
	v_add_u32_e32 v59, v59, v60
	v_subrev_u32_e32 v61, 16, v54
	v_lshlrev_b32_e32 v61, 2, v61
	ds_bpermute_b32 v60, v61, v59
	v_cmp_le_u32_e32 vcc, 16, v54
	s_waitcnt lgkmcnt(0)
	v_cndmask_b32_e32 v60, 0, v60, vcc
	v_add_u32_e32 v59, v59, v60
	v_subrev_u32_e32 v61, 32, v54
	v_lshlrev_b32_e32 v61, 2, v61
	ds_bpermute_b32 v60, v61, v59
	v_cmp_le_u32_e32 vcc, 32, v54
	s_waitcnt lgkmcnt(0)
	v_cndmask_b32_e32 v60, 0, v60, vcc
	v_add_u32_e32 v59, v59, v60
	v_lshlrev_b32_e32 v61, 2, v55
	v_cmp_eq_u32_e32 vcc, 63, v54
	s_and_saveexec_b64 s[4:5], vcc
	ds_write_b32 v61, v59 offset:16384
	s_or_b64 exec, exec, s[4:5]
	s_waitcnt lgkmcnt(0)
	s_barrier
	v_mov_b32_e32 v54, 0
	v_mov_b32_e32 v61, 0
	ds_read_b128 v[60:63], v61 offset:16384
	s_waitcnt lgkmcnt(0)
	v_cmp_lt_u32_e32 vcc, 0, v55
	s_nop 1
	v_cndmask_b32_e32 v60, 0, v60, vcc
	v_add_u32_e32 v54, v54, v60
	v_cmp_lt_u32_e32 vcc, 1, v55
	s_nop 1
	v_cndmask_b32_e32 v61, 0, v61, vcc
	v_add_u32_e32 v54, v54, v61
	v_cmp_lt_u32_e32 vcc, 2, v55
	s_nop 1
	v_cndmask_b32_e32 v62, 0, v62, vcc
	v_add_u32_e32 v54, v54, v62
	v_cmp_lt_u32_e32 vcc, 3, v55
	s_nop 1
	v_cndmask_b32_e32 v63, 0, v63, vcc
	v_add_u32_e32 v54, v54, v63
	v_mov_b32_e32 v61, 0
	ds_read_b128 v[60:63], v61 offset:16400
	s_waitcnt lgkmcnt(0)
	v_cmp_lt_u32_e32 vcc, 4, v55
	s_nop 1
	v_cndmask_b32_e32 v60, 0, v60, vcc
	v_add_u32_e32 v54, v54, v60
	v_cmp_lt_u32_e32 vcc, 5, v55
	s_nop 1
	v_cndmask_b32_e32 v61, 0, v61, vcc
	v_add_u32_e32 v54, v54, v61
	v_cmp_lt_u32_e32 vcc, 6, v55
	s_nop 1
	v_cndmask_b32_e32 v62, 0, v62, vcc
	v_add_u32_e32 v54, v54, v62
	v_cmp_lt_u32_e32 vcc, 7, v55
	s_nop 1
	v_cndmask_b32_e32 v63, 0, v63, vcc
	v_add_u32_e32 v54, v54, v63
	v_mov_b32_e32 v61, 0
	ds_read_b128 v[60:63], v61 offset:16416
	s_waitcnt lgkmcnt(0)
	v_cmp_lt_u32_e32 vcc, 8, v55
	s_nop 1
	v_cndmask_b32_e32 v60, 0, v60, vcc
	v_add_u32_e32 v54, v54, v60
	v_cmp_lt_u32_e32 vcc, 9, v55
	s_nop 1
	v_cndmask_b32_e32 v61, 0, v61, vcc
	v_add_u32_e32 v54, v54, v61
	v_cmp_lt_u32_e32 vcc, 10, v55
	s_nop 1
	v_cndmask_b32_e32 v62, 0, v62, vcc
	v_add_u32_e32 v54, v54, v62
	v_cmp_lt_u32_e32 vcc, 11, v55
	s_nop 1
	v_cndmask_b32_e32 v63, 0, v63, vcc
	v_add_u32_e32 v54, v54, v63
	v_mov_b32_e32 v61, 0
	ds_read_b128 v[60:63], v61 offset:16432
	s_waitcnt lgkmcnt(0)
	v_cmp_lt_u32_e32 vcc, 12, v55
	s_nop 1
	v_cndmask_b32_e32 v60, 0, v60, vcc
	v_add_u32_e32 v54, v54, v60
	v_cmp_lt_u32_e32 vcc, 13, v55
	s_nop 1
	v_cndmask_b32_e32 v61, 0, v61, vcc
	v_add_u32_e32 v54, v54, v61
	v_cmp_lt_u32_e32 vcc, 14, v55
	s_nop 1
	v_cndmask_b32_e32 v62, 0, v62, vcc
	v_add_u32_e32 v54, v54, v62
	v_mov_b32_e32 v62, v54
	v_sub_u32_e32 v59, v59, v58
	v_add_u32_e32 v59, v59, v62
	v_add_u32_e32 v60, v59, v50
	v_add_u32_e32 v61, v59, v56
	v_add_u32_e32 v62, v59, v57
	v_mov_b32_e32 v50, v59
	v_mov_b32_e32 v51, v60
	v_mov_b32_e32 v52, v61
	v_mov_b32_e32 v53, v62
	ds_write_b128 v1, v[50:53]
	v_and_b32_e32 v56, 7, v0
	v_lshrrev_b32_e32 v57, 3, v0
	v_lshl_add_u32 v57, s42, 7, v57
	v_cmp_eq_u32_e32 vcc, 0, v56
	v_cmp_gt_i32_e64 s[4:5], s44, v57
	s_and_b64 s[4:5], vcc, s[4:5]
	v_add_u32_e32 v58, s36, v59
	v_lshlrev_b32_e32 v56, 2, v57
	s_and_saveexec_b64 s[10:11], s[4:5]
	global_store_dword v56, v58, s[38:39]
	s_add_i32 s7, s44, -1
	v_cmp_eq_u32_e32 vcc, s7, v57
	s_and_b64 exec, exec, vcc
	v_mov_b32_e32 v58, s45
	global_store_dword v56, v58, s[38:39] offset:4
	s_mov_b64 exec, s[10:11]
	s_waitcnt lgkmcnt(0)
	s_barrier
	v_lshrrev_b32_e32 v54, 25, v2
	v_mul_u32_u24_e32 v55, 0xdf, v2
	v_lshrrev_b32_e32 v55, 20, v55
	v_min_u32_e32 v55, 31, v55
	v_xor_b32_e32 v55, s8, v55
	v_lshl_or_b32 v54, v54, 5, v55
	v_lshlrev_b32_e32 v56, 2, v54
	ds_read_b32 v56, v56
	v_lshrrev_b32_e32 v54, 25, v4
	v_mul_u32_u24_e32 v55, 0xdf, v4
	v_lshrrev_b32_e32 v55, 20, v55
	v_min_u32_e32 v55, 31, v55
	v_xor_b32_e32 v55, s8, v55
	v_lshl_or_b32 v54, v54, 5, v55
	v_lshlrev_b32_e32 v57, 2, v54
	ds_read_b32 v57, v57
	v_lshrrev_b32_e32 v54, 25, v6
	v_mul_u32_u24_e32 v55, 0xdf, v6
	v_lshrrev_b32_e32 v55, 20, v55
	v_min_u32_e32 v55, 31, v55
	v_xor_b32_e32 v55, s8, v55
	v_lshl_or_b32 v54, v54, 5, v55
	v_lshlrev_b32_e32 v58, 2, v54
	ds_read_b32 v58, v58
	v_lshrrev_b32_e32 v54, 25, v8
	v_mul_u32_u24_e32 v55, 0xdf, v8
	v_lshrrev_b32_e32 v55, 20, v55
	v_min_u32_e32 v55, 31, v55
	v_xor_b32_e32 v55, s8, v55
	v_lshl_or_b32 v54, v54, 5, v55
	v_lshlrev_b32_e32 v59, 2, v54
	ds_read_b32 v59, v59
	s_waitcnt lgkmcnt(0)
	v_add_u32_e32 v34, v34, v56
	v_and_b32_e32 v2, 0x1ffffff, v2
	v_add_u32_e32 v35, v35, v57
	v_and_b32_e32 v4, 0x1ffffff, v4
	v_add_u32_e32 v36, v36, v58
	v_and_b32_e32 v6, 0x1ffffff, v6
	v_add_u32_e32 v37, v37, v59
	v_and_b32_e32 v8, 0x1ffffff, v8
	v_lshrrev_b32_e32 v54, 25, v10
	v_mul_u32_u24_e32 v55, 0xdf, v10
	v_lshrrev_b32_e32 v55, 20, v55
	v_min_u32_e32 v55, 31, v55
	v_xor_b32_e32 v55, s8, v55
	v_lshl_or_b32 v54, v54, 5, v55
	v_lshlrev_b32_e32 v56, 2, v54
	ds_read_b32 v56, v56
	v_lshrrev_b32_e32 v54, 25, v12
	v_mul_u32_u24_e32 v55, 0xdf, v12
	v_lshrrev_b32_e32 v55, 20, v55
	v_min_u32_e32 v55, 31, v55
	v_xor_b32_e32 v55, s8, v55
	v_lshl_or_b32 v54, v54, 5, v55
	v_lshlrev_b32_e32 v57, 2, v54
	ds_read_b32 v57, v57
	v_lshrrev_b32_e32 v54, 25, v14
	v_mul_u32_u24_e32 v55, 0xdf, v14
	v_lshrrev_b32_e32 v55, 20, v55
	v_min_u32_e32 v55, 31, v55
	v_xor_b32_e32 v55, s8, v55
	v_lshl_or_b32 v54, v54, 5, v55
	v_lshlrev_b32_e32 v58, 2, v54
	ds_read_b32 v58, v58
	v_lshrrev_b32_e32 v54, 25, v16
	v_mul_u32_u24_e32 v55, 0xdf, v16
	v_lshrrev_b32_e32 v55, 20, v55
	v_min_u32_e32 v55, 31, v55
	v_xor_b32_e32 v55, s8, v55
	v_lshl_or_b32 v54, v54, 5, v55
	v_lshlrev_b32_e32 v59, 2, v54
	ds_read_b32 v59, v59
	s_waitcnt lgkmcnt(0)
	v_add_u32_e32 v38, v38, v56
	v_and_b32_e32 v10, 0x1ffffff, v10
	v_add_u32_e32 v39, v39, v57
	v_and_b32_e32 v12, 0x1ffffff, v12
	v_add_u32_e32 v40, v40, v58
	v_and_b32_e32 v14, 0x1ffffff, v14
	v_add_u32_e32 v41, v41, v59
	v_and_b32_e32 v16, 0x1ffffff, v16
	v_lshrrev_b32_e32 v54, 25, v18
	v_mul_u32_u24_e32 v55, 0xdf, v18
	v_lshrrev_b32_e32 v55, 20, v55
	v_min_u32_e32 v55, 31, v55
	v_xor_b32_e32 v55, s8, v55
	v_lshl_or_b32 v54, v54, 5, v55
	v_lshlrev_b32_e32 v56, 2, v54
	ds_read_b32 v56, v56
	v_lshrrev_b32_e32 v54, 25, v20
	v_mul_u32_u24_e32 v55, 0xdf, v20
	v_lshrrev_b32_e32 v55, 20, v55
	v_min_u32_e32 v55, 31, v55
	v_xor_b32_e32 v55, s8, v55
	v_lshl_or_b32 v54, v54, 5, v55
	v_lshlrev_b32_e32 v57, 2, v54
	ds_read_b32 v57, v57
	v_lshrrev_b32_e32 v54, 25, v22
	v_mul_u32_u24_e32 v55, 0xdf, v22
	v_lshrrev_b32_e32 v55, 20, v55
	v_min_u32_e32 v55, 31, v55
	v_xor_b32_e32 v55, s8, v55
	v_lshl_or_b32 v54, v54, 5, v55
	v_lshlrev_b32_e32 v58, 2, v54
	ds_read_b32 v58, v58
	v_lshrrev_b32_e32 v54, 25, v24
	v_mul_u32_u24_e32 v55, 0xdf, v24
	v_lshrrev_b32_e32 v55, 20, v55
	v_min_u32_e32 v55, 31, v55
	v_xor_b32_e32 v55, s8, v55
	v_lshl_or_b32 v54, v54, 5, v55
	v_lshlrev_b32_e32 v59, 2, v54
	ds_read_b32 v59, v59
	s_waitcnt lgkmcnt(0)
	v_add_u32_e32 v42, v42, v56
	v_and_b32_e32 v18, 0x1ffffff, v18
	v_add_u32_e32 v43, v43, v57
	v_and_b32_e32 v20, 0x1ffffff, v20
	v_add_u32_e32 v44, v44, v58
	v_and_b32_e32 v22, 0x1ffffff, v22
	v_add_u32_e32 v45, v45, v59
	v_and_b32_e32 v24, 0x1ffffff, v24
	v_lshrrev_b32_e32 v54, 25, v26
	v_mul_u32_u24_e32 v55, 0xdf, v26
	v_lshrrev_b32_e32 v55, 20, v55
	v_min_u32_e32 v55, 31, v55
	v_xor_b32_e32 v55, s8, v55
	v_lshl_or_b32 v54, v54, 5, v55
	v_lshlrev_b32_e32 v56, 2, v54
	ds_read_b32 v56, v56
	v_lshrrev_b32_e32 v54, 25, v28
	v_mul_u32_u24_e32 v55, 0xdf, v28
	v_lshrrev_b32_e32 v55, 20, v55
	v_min_u32_e32 v55, 31, v55
	v_xor_b32_e32 v55, s8, v55
	v_lshl_or_b32 v54, v54, 5, v55
	v_lshlrev_b32_e32 v57, 2, v54
	ds_read_b32 v57, v57
	v_lshrrev_b32_e32 v54, 25, v30
	v_mul_u32_u24_e32 v55, 0xdf, v30
	v_lshrrev_b32_e32 v55, 20, v55
	v_min_u32_e32 v55, 31, v55
	v_xor_b32_e32 v55, s8, v55
	v_lshl_or_b32 v54, v54, 5, v55
	v_lshlrev_b32_e32 v58, 2, v54
	ds_read_b32 v58, v58
	v_lshrrev_b32_e32 v54, 25, v32
	v_mul_u32_u24_e32 v55, 0xdf, v32
	v_lshrrev_b32_e32 v55, 20, v55
	v_min_u32_e32 v55, 31, v55
	v_xor_b32_e32 v55, s8, v55
	v_lshl_or_b32 v54, v54, 5, v55
	v_lshlrev_b32_e32 v59, 2, v54
	ds_read_b32 v59, v59
	s_waitcnt lgkmcnt(0)
	v_add_u32_e32 v46, v46, v56
	v_and_b32_e32 v26, 0x1ffffff, v26
	v_add_u32_e32 v47, v47, v57
	v_and_b32_e32 v28, 0x1ffffff, v28
	v_add_u32_e32 v48, v48, v58
	v_and_b32_e32 v30, 0x1ffffff, v30
	v_add_u32_e32 v49, v49, v59
	v_and_b32_e32 v32, 0x1ffffff, v32
	s_movk_i32 s14, 8000
	v_add_u32_e32 v54, 0, v0
	v_lshl_add_u32 v54, v54, 1, 0
	v_cmp_gt_i32_e32 vcc, s33, v54
	v_mov_b32_e32 v56, v34
	v_cmp_gt_u32_e64 s[4:5], s14, v56
	s_and_b64 vcc, vcc, s[4:5]
	v_lshlrev_b32_e32 v56, 3, v56
	s_and_saveexec_b64 s[4:5], vcc
	ds_write_b64 v56, v[2:3] offset:16448
	s_or_b64 exec, exec, s[4:5]
	v_add_u32_e32 v54, 0, v0
	v_lshl_add_u32 v54, v54, 1, 1
	v_cmp_gt_i32_e32 vcc, s33, v54
	v_mov_b32_e32 v56, v35
	v_cmp_gt_u32_e64 s[4:5], s14, v56
	s_and_b64 vcc, vcc, s[4:5]
	v_lshlrev_b32_e32 v56, 3, v56
	s_and_saveexec_b64 s[4:5], vcc
	ds_write_b64 v56, v[4:5] offset:16448
	s_or_b64 exec, exec, s[4:5]
	v_add_u32_e32 v54, 1024, v0
	v_lshl_add_u32 v54, v54, 1, 0
	v_cmp_gt_i32_e32 vcc, s33, v54
	v_mov_b32_e32 v56, v36
	v_cmp_gt_u32_e64 s[4:5], s14, v56
	s_and_b64 vcc, vcc, s[4:5]
	v_lshlrev_b32_e32 v56, 3, v56
	s_and_saveexec_b64 s[4:5], vcc
	ds_write_b64 v56, v[6:7] offset:16448
	s_or_b64 exec, exec, s[4:5]
	v_add_u32_e32 v54, 1024, v0
	v_lshl_add_u32 v54, v54, 1, 1
	v_cmp_gt_i32_e32 vcc, s33, v54
	v_mov_b32_e32 v56, v37
	v_cmp_gt_u32_e64 s[4:5], s14, v56
	s_and_b64 vcc, vcc, s[4:5]
	v_lshlrev_b32_e32 v56, 3, v56
	s_and_saveexec_b64 s[4:5], vcc
	ds_write_b64 v56, v[8:9] offset:16448
	s_or_b64 exec, exec, s[4:5]
	v_add_u32_e32 v54, 2048, v0
	v_lshl_add_u32 v54, v54, 1, 0
	v_cmp_gt_i32_e32 vcc, s33, v54
	v_mov_b32_e32 v56, v38
	v_cmp_gt_u32_e64 s[4:5], s14, v56
	s_and_b64 vcc, vcc, s[4:5]
	v_lshlrev_b32_e32 v56, 3, v56
	s_and_saveexec_b64 s[4:5], vcc
	ds_write_b64 v56, v[10:11] offset:16448
	s_or_b64 exec, exec, s[4:5]
	v_add_u32_e32 v54, 2048, v0
	v_lshl_add_u32 v54, v54, 1, 1
	v_cmp_gt_i32_e32 vcc, s33, v54
	v_mov_b32_e32 v56, v39
	v_cmp_gt_u32_e64 s[4:5], s14, v56
	s_and_b64 vcc, vcc, s[4:5]
	v_lshlrev_b32_e32 v56, 3, v56
	s_and_saveexec_b64 s[4:5], vcc
	ds_write_b64 v56, v[12:13] offset:16448
	s_or_b64 exec, exec, s[4:5]
	v_add_u32_e32 v54, 3072, v0
	v_lshl_add_u32 v54, v54, 1, 0
	v_cmp_gt_i32_e32 vcc, s33, v54
	v_mov_b32_e32 v56, v40
	v_cmp_gt_u32_e64 s[4:5], s14, v56
	s_and_b64 vcc, vcc, s[4:5]
	v_lshlrev_b32_e32 v56, 3, v56
	s_and_saveexec_b64 s[4:5], vcc
	ds_write_b64 v56, v[14:15] offset:16448
	s_or_b64 exec, exec, s[4:5]
	v_add_u32_e32 v54, 3072, v0
	v_lshl_add_u32 v54, v54, 1, 1
	v_cmp_gt_i32_e32 vcc, s33, v54
	v_mov_b32_e32 v56, v41
	v_cmp_gt_u32_e64 s[4:5], s14, v56
	s_and_b64 vcc, vcc, s[4:5]
	v_lshlrev_b32_e32 v56, 3, v56
	s_and_saveexec_b64 s[4:5], vcc
	ds_write_b64 v56, v[16:17] offset:16448
	s_or_b64 exec, exec, s[4:5]
	v_add_u32_e32 v54, 4096, v0
	v_lshl_add_u32 v54, v54, 1, 0
	v_cmp_gt_i32_e32 vcc, s33, v54
	v_mov_b32_e32 v56, v42
	v_cmp_gt_u32_e64 s[4:5], s14, v56
	s_and_b64 vcc, vcc, s[4:5]
	v_lshlrev_b32_e32 v56, 3, v56
	s_and_saveexec_b64 s[4:5], vcc
	ds_write_b64 v56, v[18:19] offset:16448
	s_or_b64 exec, exec, s[4:5]
	v_add_u32_e32 v54, 4096, v0
	v_lshl_add_u32 v54, v54, 1, 1
	v_cmp_gt_i32_e32 vcc, s33, v54
	v_mov_b32_e32 v56, v43
	v_cmp_gt_u32_e64 s[4:5], s14, v56
	s_and_b64 vcc, vcc, s[4:5]
	v_lshlrev_b32_e32 v56, 3, v56
	s_and_saveexec_b64 s[4:5], vcc
	ds_write_b64 v56, v[20:21] offset:16448
	s_or_b64 exec, exec, s[4:5]
	v_add_u32_e32 v54, 5120, v0
	v_lshl_add_u32 v54, v54, 1, 0
	v_cmp_gt_i32_e32 vcc, s33, v54
	v_mov_b32_e32 v56, v44
	v_cmp_gt_u32_e64 s[4:5], s14, v56
	s_and_b64 vcc, vcc, s[4:5]
	v_lshlrev_b32_e32 v56, 3, v56
	s_and_saveexec_b64 s[4:5], vcc
	ds_write_b64 v56, v[22:23] offset:16448
	s_or_b64 exec, exec, s[4:5]
	v_add_u32_e32 v54, 5120, v0
	v_lshl_add_u32 v54, v54, 1, 1
	v_cmp_gt_i32_e32 vcc, s33, v54
	v_mov_b32_e32 v56, v45
	v_cmp_gt_u32_e64 s[4:5], s14, v56
	s_and_b64 vcc, vcc, s[4:5]
	v_lshlrev_b32_e32 v56, 3, v56
	s_and_saveexec_b64 s[4:5], vcc
	ds_write_b64 v56, v[24:25] offset:16448
	s_or_b64 exec, exec, s[4:5]
	v_add_u32_e32 v54, 6144, v0
	v_lshl_add_u32 v54, v54, 1, 0
	v_cmp_gt_i32_e32 vcc, s33, v54
	v_mov_b32_e32 v56, v46
	v_cmp_gt_u32_e64 s[4:5], s14, v56
	s_and_b64 vcc, vcc, s[4:5]
	v_lshlrev_b32_e32 v56, 3, v56
	s_and_saveexec_b64 s[4:5], vcc
	ds_write_b64 v56, v[26:27] offset:16448
	s_or_b64 exec, exec, s[4:5]
	v_add_u32_e32 v54, 6144, v0
	v_lshl_add_u32 v54, v54, 1, 1
	v_cmp_gt_i32_e32 vcc, s33, v54
	v_mov_b32_e32 v56, v47
	v_cmp_gt_u32_e64 s[4:5], s14, v56
	s_and_b64 vcc, vcc, s[4:5]
	v_lshlrev_b32_e32 v56, 3, v56
	s_and_saveexec_b64 s[4:5], vcc
	ds_write_b64 v56, v[28:29] offset:16448
	s_or_b64 exec, exec, s[4:5]
	v_add_u32_e32 v54, 7168, v0
	v_lshl_add_u32 v54, v54, 1, 0
	v_cmp_gt_i32_e32 vcc, s33, v54
	v_mov_b32_e32 v56, v48
	v_cmp_gt_u32_e64 s[4:5], s14, v56
	s_and_b64 vcc, vcc, s[4:5]
	v_lshlrev_b32_e32 v56, 3, v56
	s_and_saveexec_b64 s[4:5], vcc
	ds_write_b64 v56, v[30:31] offset:16448
	s_or_b64 exec, exec, s[4:5]
	v_add_u32_e32 v54, 7168, v0
	v_lshl_add_u32 v54, v54, 1, 1
	v_cmp_gt_i32_e32 vcc, s33, v54
	v_mov_b32_e32 v56, v49
	v_cmp_gt_u32_e64 s[4:5], s14, v56
	s_and_b64 vcc, vcc, s[4:5]
	v_lshlrev_b32_e32 v56, 3, v56
	s_and_saveexec_b64 s[4:5], vcc
	ds_write_b64 v56, v[32:33] offset:16448
	s_or_b64 exec, exec, s[4:5]
	s_waitcnt lgkmcnt(0)
	s_barrier
	s_sub_i32 s6, s33, 0
	s_min_i32 s6, s6, 8000
	v_lshlrev_b32_e32 v59, 1, v0
	v_cmp_gt_i32_e32 vcc, s6, v59
	s_and_saveexec_b64 s[10:11], vcc
	s_cbranch_execz .Ll2_cpdone0
	v_add_u32_e32 v56, s36, v59
	v_ashrrev_i32_e32 v57, 31, v56
	v_lshl_add_u64 v[56:57], v[56:57], 3, s[40:41]
	v_lshlrev_b32_e32 v58, 4, v0
	s_mov_b64 s[4:5], 0
	s_mov_b64 s[12:13], 0x4000
